# speedup vs baseline: 1.0220x; 1.0058x over previous
_Z13stage0_kernel5TJobs6S0Args:
	s_load_dwordx16 s[4:19], s[0:1], 0x120
	s_load_dwordx16 s[36:51], s[0:1], 0x1e0
	s_add_u32 s34, s0, 0x120
	s_addc_u32 s35, s1, 0
	s_cmpk_gt_i32 s2, 0xcb
	s_waitcnt lgkmcnt(0)
	v_writelane_b32 v83, s4, 0
	s_nop 1
	v_writelane_b32 v83, s5, 1
	v_writelane_b32 v83, s6, 2
	v_writelane_b32 v83, s7, 3
	v_writelane_b32 v83, s8, 4
	v_writelane_b32 v83, s9, 5
	v_writelane_b32 v83, s10, 6
	v_writelane_b32 v83, s11, 7
	v_writelane_b32 v83, s12, 8
	v_writelane_b32 v83, s13, 9
	v_writelane_b32 v83, s14, 10
	v_writelane_b32 v83, s15, 11
	v_writelane_b32 v83, s16, 12
	v_writelane_b32 v83, s17, 13
	v_writelane_b32 v83, s18, 14
	v_writelane_b32 v83, s19, 15
	s_mov_b64 s[4:5], -1
	s_cbranch_scc0 .LBB0_116
	s_load_dword s4, s[34:35], 0x114
	s_add_i32 s3, s2, 0xffffff34
	v_writelane_b32 v83, s3, 16
	s_waitcnt lgkmcnt(0)
	s_cmp_ge_i32 s3, s4
	s_mov_b32 s3, s4
	s_mov_b64 s[4:5], -1
	s_cbranch_scc0 .LBB0_93
	s_mov_b32 s4, s3
	s_load_dword s3, s[0:1], 0x230
	s_waitcnt lgkmcnt(0)
	s_add_i32 s3, s3, s4
	v_readlane_b32 s4, v83, 16
	s_cmp_ge_i32 s4, s3
	s_mov_b64 s[4:5], -1
	s_cbranch_scc0 .LBB0_80
	s_sub_i32 s4, s2, 0xcc
	s_sub_i32 s4, s4, s3
	s_load_dwordx2 s[8:9], s[0:1], 0x198
	s_load_dwordx16 s[12:27], s[0:1], 0x1a0
	s_load_dwordx4 s[28:31], s[0:1], 0x1e0
	v_lshlrev_b32_e32 v5, 5, v0
	v_and_b32_e32 v6, 0x7f, v0
	v_lshlrev_b32_e32 v7, 2, v6
	v_lshlrev_b32_e32 v6, 4, v6
	v_and_b32_e32 v20, 63, v0
	v_lshlrev_b32_e32 v20, 2, v20
	v_and_b32_e32 v21, 15, v0
	v_lshlrev_b32_e32 v21, 2, v21
	s_waitcnt lgkmcnt(0)
	global_load_dwordx4 v[8:11], v5, s[16:17]
	global_load_dwordx4 v[12:15], v5, s[16:17] offset:16
	global_load_dwordx4 v[16:19], v6, s[26:27]
	global_load_dword v22, v7, s[12:13]
	global_load_dword v23, v20, s[14:15]
	global_load_dword v24, v21, s[22:23]
	global_load_dword v25, v21, s[24:25]
	s_waitcnt vmcnt(0)
	ds_write_b128 v5, v[8:11]
	ds_write_b128 v5, v[12:15] offset:16
	ds_write_b128 v6, v[16:19] offset:8192
	ds_write_b32 v7, v22 offset:10240
	ds_write_b32 v20, v23 offset:10752
	ds_write_b32 v21, v24 offset:11008
	ds_write_b32 v21, v25 offset:11072
	s_waitcnt lgkmcnt(0)
	s_barrier
	v_lshrrev_b32_e32 v1, 7, v0
	s_nop 0
	v_readfirstlane_b32 s33, v1
	v_and_b32_e32 v1, 0x7f, v0
	v_mul_u32_u24_e32 v7, 0x84, v1
	v_add_u32_e32 v7, 0x2c00, v7
	v_lshl_or_b32 v1, s4, 7, v1
	s_mov_b32 s5, 0x20460
	v_cmp_gt_u32_e32 vcc, s5, v1
	s_mov_b64 s[6:7], vcc
	v_min_u32_e32 v1, 0x2045f, v1
	v_mul_u32_u24_e32 v5, 12, v1
	s_mov_b32 s5, 0xf0f0f0f1
	v_mul_hi_u32 v77, v1, s5
	v_lshrrev_b32_e32 v77, 4, v77
	v_lshl_add_u32 v77, v77, 4, v77
	v_sub_u32_e32 v77, v1, v77
	v_lshlrev_b32_e32 v6, 7, v77
	global_load_dword v72, v5, s[8:9] offset:8
	v_mul_u32_u24_e32 v1, 0x480, v1
	v_and_b32_e32 v75, 31, v0
	v_bfe_u32 v76, v0, 6, 1
	v_lshl_or_b32 v20, v76, 6, v75
	v_lshl_or_b32 v21, s4, 7, v20
	v_min_u32_e32 v22, 0x2045f, v21
	v_mul_u32_u24_e32 v22, 12, v22
	v_add_u32_e32 v21, 32, v21
	v_min_u32_e32 v21, 0x2045f, v21
	v_mul_u32_u24_e32 v21, 12, v21
	global_load_dwordx3 v[2:4], v22, s[8:9]
	global_load_dwordx3 v[48:50], v21, s[8:9]
	v_mov_b32_e32 v23, v21
	v_bfe_u32 v21, v0, 5, 1
	v_lshl_or_b32 v22, v76, 4, v21
	v_lshlrev_b32_e32 v22, 2, v22
	v_mul_u32_u24_e32 v5, 0x84, v22
	v_lshl_add_u32 v5, v75, 2, v5
	v_add_u32_e32 v5, 0x2c00, v5
	v_mov_b32_e32 v76, v21
	v_mov_b32_e32 v0, v23
	v_lshlrev_b32_e32 v75, 2, v75
	v_mov_b32_e32 v84, 0x378e98ab
	v_mov_b32_e32 v85, 0xb9c68948
	v_mov_b32_e32 v86, 0x3b7cd369
	v_mov_b32_e32 v87, 0xbcc618b2
	v_mov_b32_e32 v88, 0x3dda74e4
	v_mov_b32_e32 v89, 0x3f228afd
	v_mov_b32_e32 v90, 0x3ba10414
	v_mov_b32_e32 v91, 0x3e03c728
	v_mov_b32_e32 v92, 0xbfb8aa3b
	v_mov_b32_e32 v93, 0x42ce8ed0
	v_mov_b32_e32 v94, 0xc2b17218
	v_mov_b32_e32 v95, 0x7f800000
	s_brev_b32 s0, -2
	s_lshl_b32 s1, s33, 5
	v_add_u32_e32 v73, s1, v76
	v_lshlrev_b32_e32 v74, 7, v73
	v_add_u32_e32 v74, v74, v75
	v_lshlrev_b32_e32 v73, 2, v73
	v_add_u32_e32 v73, 0x2800, v73
	s_cmp_eq_u32 s33, 0
	s_cbranch_scc0 .Lfeat_zc
	global_load_dword v40, v75, s[18:19]
	s_waitcnt vmcnt(0)
	v_mov_b32_e32 v8, v40
	v_mov_b32_e32 v9, v40
	v_mov_b32_e32 v10, v40
	v_mov_b32_e32 v11, v40
	v_mov_b32_e32 v12, v40
	v_mov_b32_e32 v13, v40
	v_mov_b32_e32 v14, v40
	v_mov_b32_e32 v15, v40
	v_mov_b32_e32 v16, v40
	v_mov_b32_e32 v17, v40
	v_mov_b32_e32 v18, v40
	v_mov_b32_e32 v19, v40
	v_mov_b32_e32 v20, v40
	v_mov_b32_e32 v21, v40
	v_mov_b32_e32 v22, v40
	v_mov_b32_e32 v23, v40
	v_mov_b32_e32 v24, v40
	v_mov_b32_e32 v25, v40
	v_mov_b32_e32 v26, v40
	v_mov_b32_e32 v27, v40
	v_mov_b32_e32 v28, v40
	v_mov_b32_e32 v29, v40
	v_mov_b32_e32 v30, v40
	v_mov_b32_e32 v31, v40
	v_mov_b32_e32 v32, v40
	v_mov_b32_e32 v33, v40
	v_mov_b32_e32 v34, v40
	v_mov_b32_e32 v35, v40
	v_mov_b32_e32 v36, v40
	v_mov_b32_e32 v37, v40
	v_mov_b32_e32 v38, v40
	v_mov_b32_e32 v39, v40
	s_branch .Lfeat_gc

.Lfeat_gc:
	s_waitcnt vmcnt(0)
	ds_read_b32 v40, v73
	ds_read_b32 v41, v73 offset:256
	ds_read_b32 v42, v73 offset:512
	ds_read_b32 v43, v74
	v_add_u32_e32 v73, 8, v73
	v_add_u32_e32 v74, 0x100, v74
	s_mov_b32 s10, 8
.Lfeat_loop_c:
	s_waitcnt lgkmcnt(0)
	ds_read_b32 v44, v73
	ds_read_b32 v45, v73 offset:256
	ds_read_b32 v46, v73 offset:512
	ds_read_b32 v47, v74
	v_add_u32_e32 v73, 8, v73
	v_add_u32_e32 v74, 0x100, v74
	v_mul_f32_e32 v77, v40, v2
	v_mul_f32_e32 v78, v41, v3
	v_add_f32_e32 v77, v77, v78
	v_add_f32_e32 v77, v42, v77
	v_mul_f32_e32 v78, 0x3f3504f3, v77
	v_mul_f32_e32 v79, v78, v78
	v_fmamk_f32 v81, v79, 0xba1345e1, v90
	v_fmaak_f32 v81, v79, v81, 0xbcdac9b8
	v_fmaak_f32 v81, v79, v81, 0x3de703be
	v_fmaak_f32 v81, v79, v81, 0xbec09330
	v_fmaak_f32 v81, v79, v81, 0x3e0375d0
	v_fma_f32 v81, |v78|, v81, |v78|
	v_cmp_nlt_f32_e64 vcc, |v78|, 1.0
	s_and_saveexec_b64 s[34:35], vcc
	s_cbranch_execz .Lfeat_nl_ca0
	v_fma_f32 v82, |v78|, v84, v85
	v_fma_f32 v82, |v78|, v82, v86
	v_fma_f32 v82, |v78|, v82, v87
	v_fma_f32 v82, |v78|, v82, v88
	v_fma_f32 v82, |v78|, v82, v89
	v_fma_f32 v82, |v78|, v82, v91
	v_fma_f32 v82, |v78|, v82, |v78|
	v_mul_f32_e32 v83, 0xbfb8aa3b, v82
	v_fma_f32 v79, v82, v92, -v83
	v_rndne_f32_e32 v81, v83
	v_fmac_f32_e32 v79, 0xb2a5705f, v82
	v_sub_f32_e32 v83, v83, v81
	v_add_f32_e32 v83, v83, v79
	v_cvt_i32_f32_e32 v79, v81
	v_exp_f32_e32 v83, v83
	v_cmp_nlt_f32_e32 vcc, v93, v82
	v_ldexp_f32 v83, v83, v79
	s_nop 0
	v_cndmask_b32_e32 v83, 0, v83, vcc
	v_cmp_ngt_f32_e32 vcc, v94, v82
	s_nop 1
	v_cndmask_b32_e32 v82, v95, v83, vcc
	v_sub_f32_e32 v81, 1.0, v82
.Lfeat_nl_ca0:
	s_mov_b64 exec, s[34:35]
	v_bfi_b32 v81, s0, v81, v78
	v_mul_f32_e32 v80, 0.5, v77
	v_add_f32_e32 v81, 1.0, v81
	v_mul_f32_e32 v80, v80, v81
	s_nop 1
	v_mfma_f32_32x32x2_f32 v[8:23], v80, v43, v[8:23]
	v_mul_f32_e32 v77, v40, v48
	v_mul_f32_e32 v78, v41, v49
	v_add_f32_e32 v77, v77, v78
	v_add_f32_e32 v77, v42, v77
	v_mul_f32_e32 v78, 0x3f3504f3, v77
	v_mul_f32_e32 v79, v78, v78
	v_fmamk_f32 v81, v79, 0xba1345e1, v90
	v_fmaak_f32 v81, v79, v81, 0xbcdac9b8
	v_fmaak_f32 v81, v79, v81, 0x3de703be
	v_fmaak_f32 v81, v79, v81, 0xbec09330
	v_fmaak_f32 v81, v79, v81, 0x3e0375d0
	v_fma_f32 v81, |v78|, v81, |v78|
	v_cmp_nlt_f32_e64 vcc, |v78|, 1.0
	s_and_saveexec_b64 s[34:35], vcc
	s_cbranch_execz .Lfeat_nl_ca1
	v_fma_f32 v82, |v78|, v84, v85
	v_fma_f32 v82, |v78|, v82, v86
	v_fma_f32 v82, |v78|, v82, v87
	v_fma_f32 v82, |v78|, v82, v88
	v_fma_f32 v82, |v78|, v82, v89
	v_fma_f32 v82, |v78|, v82, v91
	v_fma_f32 v82, |v78|, v82, |v78|
	v_mul_f32_e32 v83, 0xbfb8aa3b, v82
	v_fma_f32 v79, v82, v92, -v83
	v_rndne_f32_e32 v81, v83
	v_fmac_f32_e32 v79, 0xb2a5705f, v82
	v_sub_f32_e32 v83, v83, v81
	v_add_f32_e32 v83, v83, v79
	v_cvt_i32_f32_e32 v79, v81
	v_exp_f32_e32 v83, v83
	v_cmp_nlt_f32_e32 vcc, v93, v82
	v_ldexp_f32 v83, v83, v79
	s_nop 0
	v_cndmask_b32_e32 v83, 0, v83, vcc
	v_cmp_ngt_f32_e32 vcc, v94, v82
	s_nop 1
	v_cndmask_b32_e32 v82, v95, v83, vcc
	v_sub_f32_e32 v81, 1.0, v82
.Lfeat_nl_ca1:
	s_mov_b64 exec, s[34:35]
	v_bfi_b32 v81, s0, v81, v78
	v_mul_f32_e32 v80, 0.5, v77
	v_add_f32_e32 v81, 1.0, v81
	v_mul_f32_e32 v80, v80, v81
	s_nop 1
	v_mfma_f32_32x32x2_f32 v[24:39], v80, v43, v[24:39]
	s_waitcnt lgkmcnt(0)
	ds_read_b32 v40, v73
	ds_read_b32 v41, v73 offset:256
	ds_read_b32 v42, v73 offset:512
	ds_read_b32 v43, v74
	v_add_u32_e32 v73, 8, v73
	v_add_u32_e32 v74, 0x100, v74
	v_mul_f32_e32 v77, v44, v2
	v_mul_f32_e32 v78, v45, v3
	v_add_f32_e32 v77, v77, v78
	v_add_f32_e32 v77, v46, v77
	v_mul_f32_e32 v78, 0x3f3504f3, v77
	v_mul_f32_e32 v79, v78, v78
	v_fmamk_f32 v81, v79, 0xba1345e1, v90
	v_fmaak_f32 v81, v79, v81, 0xbcdac9b8
	v_fmaak_f32 v81, v79, v81, 0x3de703be
	v_fmaak_f32 v81, v79, v81, 0xbec09330
	v_fmaak_f32 v81, v79, v81, 0x3e0375d0
	v_fma_f32 v81, |v78|, v81, |v78|
	v_cmp_nlt_f32_e64 vcc, |v78|, 1.0
	s_and_saveexec_b64 s[34:35], vcc
	s_cbranch_execz .Lfeat_nl_cb0
	v_fma_f32 v82, |v78|, v84, v85
	v_fma_f32 v82, |v78|, v82, v86
	v_fma_f32 v82, |v78|, v82, v87
	v_fma_f32 v82, |v78|, v82, v88
	v_fma_f32 v82, |v78|, v82, v89
	v_fma_f32 v82, |v78|, v82, v91
	v_fma_f32 v82, |v78|, v82, |v78|
	v_mul_f32_e32 v83, 0xbfb8aa3b, v82
	v_fma_f32 v79, v82, v92, -v83
	v_rndne_f32_e32 v81, v83
	v_fmac_f32_e32 v79, 0xb2a5705f, v82
	v_sub_f32_e32 v83, v83, v81
	v_add_f32_e32 v83, v83, v79
	v_cvt_i32_f32_e32 v79, v81
	v_exp_f32_e32 v83, v83
	v_cmp_nlt_f32_e32 vcc, v93, v82
	v_ldexp_f32 v83, v83, v79
	s_nop 0
	v_cndmask_b32_e32 v83, 0, v83, vcc
	v_cmp_ngt_f32_e32 vcc, v94, v82
	s_nop 1
	v_cndmask_b32_e32 v82, v95, v83, vcc
	v_sub_f32_e32 v81, 1.0, v82
.Lfeat_nl_cb0:
	s_mov_b64 exec, s[34:35]
	v_bfi_b32 v81, s0, v81, v78
	v_mul_f32_e32 v80, 0.5, v77
	v_add_f32_e32 v81, 1.0, v81
	v_mul_f32_e32 v80, v80, v81
	s_nop 1
	v_mfma_f32_32x32x2_f32 v[8:23], v80, v47, v[8:23]
	v_mul_f32_e32 v77, v44, v48
	v_mul_f32_e32 v78, v45, v49
	v_add_f32_e32 v77, v77, v78
	v_add_f32_e32 v77, v46, v77
	v_mul_f32_e32 v78, 0x3f3504f3, v77
	v_mul_f32_e32 v79, v78, v78
	v_fmamk_f32 v81, v79, 0xba1345e1, v90
	v_fmaak_f32 v81, v79, v81, 0xbcdac9b8
	v_fmaak_f32 v81, v79, v81, 0x3de703be
	v_fmaak_f32 v81, v79, v81, 0xbec09330
	v_fmaak_f32 v81, v79, v81, 0x3e0375d0
	v_fma_f32 v81, |v78|, v81, |v78|
	v_cmp_nlt_f32_e64 vcc, |v78|, 1.0
	s_and_saveexec_b64 s[34:35], vcc
	s_cbranch_execz .Lfeat_nl_cb1
	v_fma_f32 v82, |v78|, v84, v85
	v_fma_f32 v82, |v78|, v82, v86
	v_fma_f32 v82, |v78|, v82, v87
	v_fma_f32 v82, |v78|, v82, v88
	v_fma_f32 v82, |v78|, v82, v89
	v_fma_f32 v82, |v78|, v82, v91
	v_fma_f32 v82, |v78|, v82, |v78|
	v_mul_f32_e32 v83, 0xbfb8aa3b, v82
	v_fma_f32 v79, v82, v92, -v83
	v_rndne_f32_e32 v81, v83
	v_fmac_f32_e32 v79, 0xb2a5705f, v82
	v_sub_f32_e32 v83, v83, v81
	v_add_f32_e32 v83, v83, v79
	v_cvt_i32_f32_e32 v79, v81
	v_exp_f32_e32 v83, v83
	v_cmp_nlt_f32_e32 vcc, v93, v82
	v_ldexp_f32 v83, v83, v79
	s_nop 0
	v_cndmask_b32_e32 v83, 0, v83, vcc
	v_cmp_ngt_f32_e32 vcc, v94, v82
	s_nop 1
	v_cndmask_b32_e32 v82, v95, v83, vcc
	v_sub_f32_e32 v81, 1.0, v82
.Lfeat_nl_cb1:
	s_mov_b64 exec, s[34:35]
	v_bfi_b32 v81, s0, v81, v78
	v_mul_f32_e32 v80, 0.5, v77
	v_add_f32_e32 v81, 1.0, v81
	v_mul_f32_e32 v80, v80, v81
	s_nop 1
	v_mfma_f32_32x32x2_f32 v[24:39], v80, v47, v[24:39]
	s_sub_u32 s10, s10, 1
	s_cmp_lg_u32 s10, 0
	s_cbranch_scc1 .Lfeat_loop_c
	s_waitcnt lgkmcnt(0)
	s_cmp_eq_u32 s33, 0
	s_cbranch_scc1 .Lfeat_c_nw
	s_nop 15
	s_nop 3
	ds_write_b32 v5, v8 offset:0
	ds_write_b32 v5, v9 offset:132
	ds_write_b32 v5, v10 offset:264
	ds_write_b32 v5, v11 offset:396
	ds_write_b32 v5, v12 offset:1056
	ds_write_b32 v5, v13 offset:1188
	ds_write_b32 v5, v14 offset:1320
	ds_write_b32 v5, v15 offset:1452
	ds_write_b32 v5, v16 offset:2112
	ds_write_b32 v5, v17 offset:2244
	ds_write_b32 v5, v18 offset:2376
	ds_write_b32 v5, v19 offset:2508
	ds_write_b32 v5, v20 offset:3168
	ds_write_b32 v5, v21 offset:3300
	ds_write_b32 v5, v22 offset:3432
	ds_write_b32 v5, v23 offset:3564
	ds_write_b32 v5, v24 offset:4224
	ds_write_b32 v5, v25 offset:4356
	ds_write_b32 v5, v26 offset:4488
	ds_write_b32 v5, v27 offset:4620
	ds_write_b32 v5, v28 offset:5280
	ds_write_b32 v5, v29 offset:5412
	ds_write_b32 v5, v30 offset:5544
	ds_write_b32 v5, v31 offset:5676
	ds_write_b32 v5, v32 offset:6336
	ds_write_b32 v5, v33 offset:6468
	ds_write_b32 v5, v34 offset:6600
	ds_write_b32 v5, v35 offset:6732
	ds_write_b32 v5, v36 offset:7392
	ds_write_b32 v5, v37 offset:7524
	ds_write_b32 v5, v38 offset:7656
	ds_write_b32 v5, v39 offset:7788
	s_waitcnt lgkmcnt(0)
.Lfeat_c_nw:
	s_barrier
	s_cmp_eq_u32 s33, 0
	s_cbranch_scc0 .Lfeat_c_nf
	ds_read_b32 v40, v5 offset:0
	ds_read_b32 v41, v5 offset:132
	ds_read_b32 v42, v5 offset:264
	ds_read_b32 v43, v5 offset:396
	ds_read_b32 v44, v5 offset:1056
	ds_read_b32 v45, v5 offset:1188
	ds_read_b32 v46, v5 offset:1320
	ds_read_b32 v47, v5 offset:1452
	ds_read_b32 v48, v5 offset:2112
	ds_read_b32 v49, v5 offset:2244
	ds_read_b32 v50, v5 offset:2376
	ds_read_b32 v51, v5 offset:2508
	ds_read_b32 v52, v5 offset:3168
	ds_read_b32 v53, v5 offset:3300
	ds_read_b32 v54, v5 offset:3432
	ds_read_b32 v55, v5 offset:3564
	ds_read_b32 v56, v5 offset:4224
	ds_read_b32 v57, v5 offset:4356
	ds_read_b32 v58, v5 offset:4488
	ds_read_b32 v59, v5 offset:4620
	ds_read_b32 v60, v5 offset:5280
	ds_read_b32 v61, v5 offset:5412
	ds_read_b32 v62, v5 offset:5544
	ds_read_b32 v63, v5 offset:5676
	ds_read_b32 v64, v5 offset:6336
	ds_read_b32 v65, v5 offset:6468
	ds_read_b32 v66, v5 offset:6600
	ds_read_b32 v67, v5 offset:6732
	ds_read_b32 v68, v5 offset:7392
	ds_read_b32 v69, v5 offset:7524
	ds_read_b32 v70, v5 offset:7656
	ds_read_b32 v71, v5 offset:7788
	s_waitcnt lgkmcnt(0)
	v_add_f32_e32 v8, v8, v40
	v_add_f32_e32 v9, v9, v41
	v_add_f32_e32 v10, v10, v42
	v_add_f32_e32 v11, v11, v43
	v_add_f32_e32 v12, v12, v44
	v_add_f32_e32 v13, v13, v45
	v_add_f32_e32 v14, v14, v46
	v_add_f32_e32 v15, v15, v47
	v_add_f32_e32 v16, v16, v48
	v_add_f32_e32 v17, v17, v49
	v_add_f32_e32 v18, v18, v50
	v_add_f32_e32 v19, v19, v51
	v_add_f32_e32 v20, v20, v52
	v_add_f32_e32 v21, v21, v53
	v_add_f32_e32 v22, v22, v54
	v_add_f32_e32 v23, v23, v55
	v_add_f32_e32 v24, v24, v56
	v_add_f32_e32 v25, v25, v57
	v_add_f32_e32 v26, v26, v58
	v_add_f32_e32 v27, v27, v59
	v_add_f32_e32 v28, v28, v60
	v_add_f32_e32 v29, v29, v61
	v_add_f32_e32 v30, v30, v62
	v_add_f32_e32 v31, v31, v63
	v_add_f32_e32 v32, v32, v64
	v_add_f32_e32 v33, v33, v65
	v_add_f32_e32 v34, v34, v66
	v_add_f32_e32 v35, v35, v67
	v_add_f32_e32 v36, v36, v68
	v_add_f32_e32 v37, v37, v69
	v_add_f32_e32 v38, v38, v70
	v_add_f32_e32 v39, v39, v71
	ds_write_b32 v5, v8 offset:0
	ds_write_b32 v5, v9 offset:132
	ds_write_b32 v5, v10 offset:264
	ds_write_b32 v5, v11 offset:396
	ds_write_b32 v5, v12 offset:1056
	ds_write_b32 v5, v13 offset:1188
	ds_write_b32 v5, v14 offset:1320
	ds_write_b32 v5, v15 offset:1452
	ds_write_b32 v5, v16 offset:2112
	ds_write_b32 v5, v17 offset:2244
	ds_write_b32 v5, v18 offset:2376
	ds_write_b32 v5, v19 offset:2508
	ds_write_b32 v5, v20 offset:3168
	ds_write_b32 v5, v21 offset:3300
	ds_write_b32 v5, v22 offset:3432
	ds_write_b32 v5, v23 offset:3564
	ds_write_b32 v5, v24 offset:4224
	ds_write_b32 v5, v25 offset:4356
	ds_write_b32 v5, v26 offset:4488
	ds_write_b32 v5, v27 offset:4620
	ds_write_b32 v5, v28 offset:5280
	ds_write_b32 v5, v29 offset:5412
	ds_write_b32 v5, v30 offset:5544
	ds_write_b32 v5, v31 offset:5676
	ds_write_b32 v5, v32 offset:6336
	ds_write_b32 v5, v33 offset:6468
	ds_write_b32 v5, v34 offset:6600
	ds_write_b32 v5, v35 offset:6732
	ds_write_b32 v5, v36 offset:7392
	ds_write_b32 v5, v37 offset:7524
	ds_write_b32 v5, v38 offset:7656
	ds_write_b32 v5, v39 offset:7788
	s_waitcnt lgkmcnt(0)
	ds_read_b32 v8, v7 offset:0
	ds_read_b32 v9, v7 offset:4
	ds_read_b32 v10, v7 offset:8
	ds_read_b32 v11, v7 offset:12
	ds_read_b32 v12, v7 offset:16
	ds_read_b32 v13, v7 offset:20
	ds_read_b32 v14, v7 offset:24
	ds_read_b32 v15, v7 offset:28
	ds_read_b32 v16, v7 offset:32
	ds_read_b32 v17, v7 offset:36
	ds_read_b32 v18, v7 offset:40
	ds_read_b32 v19, v7 offset:44
	ds_read_b32 v20, v7 offset:48
	ds_read_b32 v21, v7 offset:52
	ds_read_b32 v22, v7 offset:56
	ds_read_b32 v23, v7 offset:60
	ds_read_b32 v24, v7 offset:64
	ds_read_b32 v25, v7 offset:68
	ds_read_b32 v26, v7 offset:72
	ds_read_b32 v27, v7 offset:76
	ds_read_b32 v28, v7 offset:80
	ds_read_b32 v29, v7 offset:84
	ds_read_b32 v30, v7 offset:88
	ds_read_b32 v31, v7 offset:92
	ds_read_b32 v32, v7 offset:96
	ds_read_b32 v33, v7 offset:100
	ds_read_b32 v34, v7 offset:104
	ds_read_b32 v35, v7 offset:108
	ds_read_b32 v36, v7 offset:112
	ds_read_b32 v37, v7 offset:116
	ds_read_b32 v38, v7 offset:120
	ds_read_b32 v39, v7 offset:124
	s_waitcnt lgkmcnt(0)
	global_load_dwordx4 v[40:43], v6, s[20:21] offset:0
	global_load_dwordx4 v[44:47], v6, s[20:21] offset:16
	global_load_dwordx4 v[48:51], v6, s[20:21] offset:32
	global_load_dwordx4 v[52:55], v6, s[20:21] offset:48
	global_load_dwordx4 v[56:59], v6, s[20:21] offset:64
	global_load_dwordx4 v[60:63], v6, s[20:21] offset:80
	global_load_dwordx4 v[64:67], v6, s[20:21] offset:96
	global_load_dwordx4 v[68:71], v6, s[20:21] offset:112
	s_waitcnt vmcnt(0)
	v_cmp_lt_f32_e32 vcc, 0.5, v72
	v_add_f32_e32 v8, v8, v40
	v_add_f32_e32 v9, v9, v41
	v_add_f32_e32 v10, v10, v42
	v_add_f32_e32 v11, v11, v43
	v_add_f32_e32 v12, v12, v44
	v_add_f32_e32 v13, v13, v45
	v_add_f32_e32 v14, v14, v46
	v_add_f32_e32 v15, v15, v47
	v_add_f32_e32 v16, v16, v48
	v_add_f32_e32 v17, v17, v49
	v_add_f32_e32 v18, v18, v50
	v_add_f32_e32 v19, v19, v51
	v_add_f32_e32 v20, v20, v52
	v_add_f32_e32 v21, v21, v53
	v_add_f32_e32 v22, v22, v54
	v_add_f32_e32 v23, v23, v55
	v_add_f32_e32 v24, v24, v56
	v_add_f32_e32 v25, v25, v57
	v_add_f32_e32 v26, v26, v58
	v_add_f32_e32 v27, v27, v59
	v_add_f32_e32 v28, v28, v60
	v_add_f32_e32 v29, v29, v61
	v_add_f32_e32 v30, v30, v62
	v_add_f32_e32 v31, v31, v63
	v_add_f32_e32 v32, v32, v64
	v_add_f32_e32 v33, v33, v65
	v_add_f32_e32 v34, v34, v66
	v_add_f32_e32 v35, v35, v67
	v_add_f32_e32 v36, v36, v68
	v_add_f32_e32 v37, v37, v69
	v_add_f32_e32 v38, v38, v70
	v_add_f32_e32 v39, v39, v71
	v_cndmask_b32_e32 v8, v40, v8, vcc
	v_cndmask_b32_e32 v9, v41, v9, vcc
	v_cndmask_b32_e32 v10, v42, v10, vcc
	v_cndmask_b32_e32 v11, v43, v11, vcc
	v_cndmask_b32_e32 v12, v44, v12, vcc
	v_cndmask_b32_e32 v13, v45, v13, vcc
	v_cndmask_b32_e32 v14, v46, v14, vcc
	v_cndmask_b32_e32 v15, v47, v15, vcc
	v_cndmask_b32_e32 v16, v48, v16, vcc
	v_cndmask_b32_e32 v17, v49, v17, vcc
	v_cndmask_b32_e32 v18, v50, v18, vcc
	v_cndmask_b32_e32 v19, v51, v19, vcc
	v_cndmask_b32_e32 v20, v52, v20, vcc
	v_cndmask_b32_e32 v21, v53, v21, vcc
	v_cndmask_b32_e32 v22, v54, v22, vcc
	v_cndmask_b32_e32 v23, v55, v23, vcc
	v_cndmask_b32_e32 v24, v56, v24, vcc
	v_cndmask_b32_e32 v25, v57, v25, vcc
	v_cndmask_b32_e32 v26, v58, v26, vcc
	v_cndmask_b32_e32 v27, v59, v27, vcc
	v_cndmask_b32_e32 v28, v60, v28, vcc
	v_cndmask_b32_e32 v29, v61, v29, vcc
	v_cndmask_b32_e32 v30, v62, v30, vcc
	v_cndmask_b32_e32 v31, v63, v31, vcc
	v_cndmask_b32_e32 v32, v64, v32, vcc
	v_cndmask_b32_e32 v33, v65, v33, vcc
	v_cndmask_b32_e32 v34, v66, v34, vcc
	v_cndmask_b32_e32 v35, v67, v35, vcc
	v_cndmask_b32_e32 v36, v68, v36, vcc
	v_cndmask_b32_e32 v37, v69, v37, vcc
	v_cndmask_b32_e32 v38, v70, v38, vcc
	v_cndmask_b32_e32 v39, v71, v39, vcc
	s_mov_b64 s[34:35], exec
	s_and_b64 exec, exec, s[6:7]
	v_cvt_pk_f16_f32 v80, v8, v9
	v_cvt_pk_f16_f32 v81, v10, v11
	v_cvt_pk_f16_f32 v82, v12, v13
	v_cvt_pk_f16_f32 v83, v14, v15
	global_store_dwordx4 v1, v[80:83], s[30:31] offset:1024
	s_nop 1
	v_cvt_pk_f16_f32 v80, v16, v17
	v_cvt_pk_f16_f32 v81, v18, v19
	v_cvt_pk_f16_f32 v82, v20, v21
	v_cvt_pk_f16_f32 v83, v22, v23
	global_store_dwordx4 v1, v[80:83], s[30:31] offset:1040
	s_nop 1
	v_cvt_pk_f16_f32 v80, v24, v25
	v_cvt_pk_f16_f32 v81, v26, v27
	v_cvt_pk_f16_f32 v82, v28, v29
	v_cvt_pk_f16_f32 v83, v30, v31
	global_store_dwordx4 v1, v[80:83], s[30:31] offset:1056
	s_nop 1
	v_cvt_pk_f16_f32 v80, v32, v33
	v_cvt_pk_f16_f32 v81, v34, v35
	v_cvt_pk_f16_f32 v82, v36, v37
	v_cvt_pk_f16_f32 v83, v38, v39
	global_store_dwordx4 v1, v[80:83], s[30:31] offset:1072
	s_mov_b64 exec, s[34:35]
	s_nop 1
.Lfeat_c_nf:
	global_load_dwordx3 v[48:50], v0, s[8:9]
	s_lshl_b32 s1, s33, 3
	v_add_u32_e32 v73, s1, v76
	v_lshlrev_b32_e32 v74, 7, v73
	v_add_u32_e32 v74, v74, v75
	v_add_u32_e32 v74, 0x2000, v74
	v_lshlrev_b32_e32 v73, 2, v73
	v_add_u32_e32 v73, 0x2b00, v73
	s_cmp_eq_u32 s33, 0
	s_cbranch_scc0 .Lfeat_zf
	global_load_dword v40, v75, s[28:29]
	s_waitcnt vmcnt(0)
	v_mov_b32_e32 v8, v40
	v_mov_b32_e32 v9, v40
	v_mov_b32_e32 v10, v40
	v_mov_b32_e32 v11, v40
	v_mov_b32_e32 v12, v40
	v_mov_b32_e32 v13, v40
	v_mov_b32_e32 v14, v40
	v_mov_b32_e32 v15, v40
	v_mov_b32_e32 v16, v40
	v_mov_b32_e32 v17, v40
	v_mov_b32_e32 v18, v40
	v_mov_b32_e32 v19, v40
	v_mov_b32_e32 v20, v40
	v_mov_b32_e32 v21, v40
	v_mov_b32_e32 v22, v40
	v_mov_b32_e32 v23, v40
	v_mov_b32_e32 v24, v40
	v_mov_b32_e32 v25, v40
	v_mov_b32_e32 v26, v40
	v_mov_b32_e32 v27, v40
	v_mov_b32_e32 v28, v40
	v_mov_b32_e32 v29, v40
	v_mov_b32_e32 v30, v40
	v_mov_b32_e32 v31, v40
	v_mov_b32_e32 v32, v40
	v_mov_b32_e32 v33, v40
	v_mov_b32_e32 v34, v40
	v_mov_b32_e32 v35, v40
	v_mov_b32_e32 v36, v40
	v_mov_b32_e32 v37, v40
	v_mov_b32_e32 v38, v40
	v_mov_b32_e32 v39, v40
	s_branch .Lfeat_gf

.Lfeat_gf:
	s_waitcnt vmcnt(0)
	ds_read_b32 v40, v73
	ds_read_b32 v42, v73 offset:64
	ds_read_b32 v43, v74
	v_add_u32_e32 v73, 8, v73
	v_add_u32_e32 v74, 0x100, v74
	s_mov_b32 s10, 2
.Lfeat_loop_f:
	s_waitcnt lgkmcnt(0)
	ds_read_b32 v44, v73
	ds_read_b32 v46, v73 offset:64
	ds_read_b32 v47, v74
	v_add_u32_e32 v73, 8, v73
	v_add_u32_e32 v74, 0x100, v74
	v_fma_f32 v77, v40, v4, v42
	v_mul_f32_e32 v78, 0x3f3504f3, v77
	v_mul_f32_e32 v79, v78, v78
	v_fmamk_f32 v81, v79, 0xba1345e1, v90
	v_fmaak_f32 v81, v79, v81, 0xbcdac9b8
	v_fmaak_f32 v81, v79, v81, 0x3de703be
	v_fmaak_f32 v81, v79, v81, 0xbec09330
	v_fmaak_f32 v81, v79, v81, 0x3e0375d0
	v_fma_f32 v81, |v78|, v81, |v78|
	v_cmp_nlt_f32_e64 vcc, |v78|, 1.0
	s_and_saveexec_b64 s[34:35], vcc
	s_cbranch_execz .Lfeat_nl_fa0
	v_fma_f32 v82, |v78|, v84, v85
	v_fma_f32 v82, |v78|, v82, v86
	v_fma_f32 v82, |v78|, v82, v87
	v_fma_f32 v82, |v78|, v82, v88
	v_fma_f32 v82, |v78|, v82, v89
	v_fma_f32 v82, |v78|, v82, v91
	v_fma_f32 v82, |v78|, v82, |v78|
	v_mul_f32_e32 v83, 0xbfb8aa3b, v82
	v_fma_f32 v79, v82, v92, -v83
	v_rndne_f32_e32 v81, v83
	v_fmac_f32_e32 v79, 0xb2a5705f, v82
	v_sub_f32_e32 v83, v83, v81
	v_add_f32_e32 v83, v83, v79
	v_cvt_i32_f32_e32 v79, v81
	v_exp_f32_e32 v83, v83
	v_cmp_nlt_f32_e32 vcc, v93, v82
	v_ldexp_f32 v83, v83, v79
	s_nop 0
	v_cndmask_b32_e32 v83, 0, v83, vcc
	v_cmp_ngt_f32_e32 vcc, v94, v82
	s_nop 1
	v_cndmask_b32_e32 v82, v95, v83, vcc
	v_sub_f32_e32 v81, 1.0, v82
.Lfeat_nl_fa0:
	s_mov_b64 exec, s[34:35]
	v_bfi_b32 v81, s0, v81, v78
	v_mul_f32_e32 v80, 0.5, v77
	v_add_f32_e32 v81, 1.0, v81
	v_mul_f32_e32 v80, v80, v81
	s_nop 1
	v_mfma_f32_32x32x2_f32 v[8:23], v80, v43, v[8:23]
	v_fma_f32 v77, v40, v50, v42
	v_mul_f32_e32 v78, 0x3f3504f3, v77
	v_mul_f32_e32 v79, v78, v78
	v_fmamk_f32 v81, v79, 0xba1345e1, v90
	v_fmaak_f32 v81, v79, v81, 0xbcdac9b8
	v_fmaak_f32 v81, v79, v81, 0x3de703be
	v_fmaak_f32 v81, v79, v81, 0xbec09330
	v_fmaak_f32 v81, v79, v81, 0x3e0375d0
	v_fma_f32 v81, |v78|, v81, |v78|
	v_cmp_nlt_f32_e64 vcc, |v78|, 1.0
	s_and_saveexec_b64 s[34:35], vcc
	s_cbranch_execz .Lfeat_nl_fa1
	v_fma_f32 v82, |v78|, v84, v85
	v_fma_f32 v82, |v78|, v82, v86
	v_fma_f32 v82, |v78|, v82, v87
	v_fma_f32 v82, |v78|, v82, v88
	v_fma_f32 v82, |v78|, v82, v89
	v_fma_f32 v82, |v78|, v82, v91
	v_fma_f32 v82, |v78|, v82, |v78|
	v_mul_f32_e32 v83, 0xbfb8aa3b, v82
	v_fma_f32 v79, v82, v92, -v83
	v_rndne_f32_e32 v81, v83
	v_fmac_f32_e32 v79, 0xb2a5705f, v82
	v_sub_f32_e32 v83, v83, v81
	v_add_f32_e32 v83, v83, v79
	v_cvt_i32_f32_e32 v79, v81
	v_exp_f32_e32 v83, v83
	v_cmp_nlt_f32_e32 vcc, v93, v82
	v_ldexp_f32 v83, v83, v79
	s_nop 0
	v_cndmask_b32_e32 v83, 0, v83, vcc
	v_cmp_ngt_f32_e32 vcc, v94, v82
	s_nop 1
	v_cndmask_b32_e32 v82, v95, v83, vcc
	v_sub_f32_e32 v81, 1.0, v82
.Lfeat_nl_fa1:
	s_mov_b64 exec, s[34:35]
	v_bfi_b32 v81, s0, v81, v78
	v_mul_f32_e32 v80, 0.5, v77
	v_add_f32_e32 v81, 1.0, v81
	v_mul_f32_e32 v80, v80, v81
	s_nop 1
	v_mfma_f32_32x32x2_f32 v[24:39], v80, v43, v[24:39]
	s_waitcnt lgkmcnt(0)
	ds_read_b32 v40, v73
	ds_read_b32 v42, v73 offset:64
	ds_read_b32 v43, v74
	v_add_u32_e32 v73, 8, v73
	v_add_u32_e32 v74, 0x100, v74
	v_fma_f32 v77, v44, v4, v46
	v_mul_f32_e32 v78, 0x3f3504f3, v77
	v_mul_f32_e32 v79, v78, v78
	v_fmamk_f32 v81, v79, 0xba1345e1, v90
	v_fmaak_f32 v81, v79, v81, 0xbcdac9b8
	v_fmaak_f32 v81, v79, v81, 0x3de703be
	v_fmaak_f32 v81, v79, v81, 0xbec09330
	v_fmaak_f32 v81, v79, v81, 0x3e0375d0
	v_fma_f32 v81, |v78|, v81, |v78|
	v_cmp_nlt_f32_e64 vcc, |v78|, 1.0
	s_and_saveexec_b64 s[34:35], vcc
	s_cbranch_execz .Lfeat_nl_fb0
	v_fma_f32 v82, |v78|, v84, v85
	v_fma_f32 v82, |v78|, v82, v86
	v_fma_f32 v82, |v78|, v82, v87
	v_fma_f32 v82, |v78|, v82, v88
	v_fma_f32 v82, |v78|, v82, v89
	v_fma_f32 v82, |v78|, v82, v91
	v_fma_f32 v82, |v78|, v82, |v78|
	v_mul_f32_e32 v83, 0xbfb8aa3b, v82
	v_fma_f32 v79, v82, v92, -v83
	v_rndne_f32_e32 v81, v83
	v_fmac_f32_e32 v79, 0xb2a5705f, v82
	v_sub_f32_e32 v83, v83, v81
	v_add_f32_e32 v83, v83, v79
	v_cvt_i32_f32_e32 v79, v81
	v_exp_f32_e32 v83, v83
	v_cmp_nlt_f32_e32 vcc, v93, v82
	v_ldexp_f32 v83, v83, v79
	s_nop 0
	v_cndmask_b32_e32 v83, 0, v83, vcc
	v_cmp_ngt_f32_e32 vcc, v94, v82
	s_nop 1
	v_cndmask_b32_e32 v82, v95, v83, vcc
	v_sub_f32_e32 v81, 1.0, v82
.Lfeat_nl_fb0:
	s_mov_b64 exec, s[34:35]
	v_bfi_b32 v81, s0, v81, v78
	v_mul_f32_e32 v80, 0.5, v77
	v_add_f32_e32 v81, 1.0, v81
	v_mul_f32_e32 v80, v80, v81
	s_nop 1
	v_mfma_f32_32x32x2_f32 v[8:23], v80, v47, v[8:23]
	v_fma_f32 v77, v44, v50, v46
	v_mul_f32_e32 v78, 0x3f3504f3, v77
	v_mul_f32_e32 v79, v78, v78
	v_fmamk_f32 v81, v79, 0xba1345e1, v90
	v_fmaak_f32 v81, v79, v81, 0xbcdac9b8
	v_fmaak_f32 v81, v79, v81, 0x3de703be
	v_fmaak_f32 v81, v79, v81, 0xbec09330
	v_fmaak_f32 v81, v79, v81, 0x3e0375d0
	v_fma_f32 v81, |v78|, v81, |v78|
	v_cmp_nlt_f32_e64 vcc, |v78|, 1.0
	s_and_saveexec_b64 s[34:35], vcc
	s_cbranch_execz .Lfeat_nl_fb1
	v_fma_f32 v82, |v78|, v84, v85
	v_fma_f32 v82, |v78|, v82, v86
	v_fma_f32 v82, |v78|, v82, v87
	v_fma_f32 v82, |v78|, v82, v88
	v_fma_f32 v82, |v78|, v82, v89
	v_fma_f32 v82, |v78|, v82, v91
	v_fma_f32 v82, |v78|, v82, |v78|
	v_mul_f32_e32 v83, 0xbfb8aa3b, v82
	v_fma_f32 v79, v82, v92, -v83
	v_rndne_f32_e32 v81, v83
	v_fmac_f32_e32 v79, 0xb2a5705f, v82
	v_sub_f32_e32 v83, v83, v81
	v_add_f32_e32 v83, v83, v79
	v_cvt_i32_f32_e32 v79, v81
	v_exp_f32_e32 v83, v83
	v_cmp_nlt_f32_e32 vcc, v93, v82
	v_ldexp_f32 v83, v83, v79
	s_nop 0
	v_cndmask_b32_e32 v83, 0, v83, vcc
	v_cmp_ngt_f32_e32 vcc, v94, v82
	s_nop 1
	v_cndmask_b32_e32 v82, v95, v83, vcc
	v_sub_f32_e32 v81, 1.0, v82
.Lfeat_nl_fb1:
	s_mov_b64 exec, s[34:35]
	v_bfi_b32 v81, s0, v81, v78
	v_mul_f32_e32 v80, 0.5, v77
	v_add_f32_e32 v81, 1.0, v81
	v_mul_f32_e32 v80, v80, v81
	s_nop 1
	v_mfma_f32_32x32x2_f32 v[24:39], v80, v47, v[24:39]
	s_sub_u32 s10, s10, 1
	s_cmp_lg_u32 s10, 0
	s_cbranch_scc1 .Lfeat_loop_f
	s_waitcnt lgkmcnt(0)
	s_nop 15
	s_nop 3
	s_cmp_eq_u32 s33, 0
	s_cbranch_scc0 .Lfeat_f_nw
	ds_write_b32 v5, v8 offset:0
	ds_write_b32 v5, v9 offset:132
	ds_write_b32 v5, v10 offset:264
	ds_write_b32 v5, v11 offset:396
	ds_write_b32 v5, v12 offset:1056
	ds_write_b32 v5, v13 offset:1188
	ds_write_b32 v5, v14 offset:1320
	ds_write_b32 v5, v15 offset:1452
	ds_write_b32 v5, v16 offset:2112
	ds_write_b32 v5, v17 offset:2244
	ds_write_b32 v5, v18 offset:2376
	ds_write_b32 v5, v19 offset:2508
	ds_write_b32 v5, v20 offset:3168
	ds_write_b32 v5, v21 offset:3300
	ds_write_b32 v5, v22 offset:3432
	ds_write_b32 v5, v23 offset:3564
	ds_write_b32 v5, v24 offset:4224
	ds_write_b32 v5, v25 offset:4356
	ds_write_b32 v5, v26 offset:4488
	ds_write_b32 v5, v27 offset:4620
	ds_write_b32 v5, v28 offset:5280
	ds_write_b32 v5, v29 offset:5412
	ds_write_b32 v5, v30 offset:5544
	ds_write_b32 v5, v31 offset:5676
	ds_write_b32 v5, v32 offset:6336
	ds_write_b32 v5, v33 offset:6468
	ds_write_b32 v5, v34 offset:6600
	ds_write_b32 v5, v35 offset:6732
	ds_write_b32 v5, v36 offset:7392
	ds_write_b32 v5, v37 offset:7524
	ds_write_b32 v5, v38 offset:7656
	ds_write_b32 v5, v39 offset:7788
	s_waitcnt lgkmcnt(0)
.Lfeat_f_nw:
	s_barrier
	s_cmp_eq_u32 s33, 0
	s_cbranch_scc1 .Lfeat_done
	ds_read_b32 v40, v5 offset:0
	ds_read_b32 v41, v5 offset:132
	ds_read_b32 v42, v5 offset:264
	ds_read_b32 v43, v5 offset:396
	ds_read_b32 v44, v5 offset:1056
	ds_read_b32 v45, v5 offset:1188
	ds_read_b32 v46, v5 offset:1320
	ds_read_b32 v47, v5 offset:1452
	ds_read_b32 v48, v5 offset:2112
	ds_read_b32 v49, v5 offset:2244
	ds_read_b32 v50, v5 offset:2376
	ds_read_b32 v51, v5 offset:2508
	ds_read_b32 v52, v5 offset:3168
	ds_read_b32 v53, v5 offset:3300
	ds_read_b32 v54, v5 offset:3432
	ds_read_b32 v55, v5 offset:3564
	ds_read_b32 v56, v5 offset:4224
	ds_read_b32 v57, v5 offset:4356
	ds_read_b32 v58, v5 offset:4488
	ds_read_b32 v59, v5 offset:4620
	ds_read_b32 v60, v5 offset:5280
	ds_read_b32 v61, v5 offset:5412
	ds_read_b32 v62, v5 offset:5544
	ds_read_b32 v63, v5 offset:5676
	ds_read_b32 v64, v5 offset:6336
	ds_read_b32 v65, v5 offset:6468
	ds_read_b32 v66, v5 offset:6600
	ds_read_b32 v67, v5 offset:6732
	ds_read_b32 v68, v5 offset:7392
	ds_read_b32 v69, v5 offset:7524
	ds_read_b32 v70, v5 offset:7656
	ds_read_b32 v71, v5 offset:7788
	s_waitcnt lgkmcnt(0)
	v_add_f32_e32 v8, v8, v40
	v_add_f32_e32 v9, v9, v41
	v_add_f32_e32 v10, v10, v42
	v_add_f32_e32 v11, v11, v43
	v_add_f32_e32 v12, v12, v44
	v_add_f32_e32 v13, v13, v45
	v_add_f32_e32 v14, v14, v46
	v_add_f32_e32 v15, v15, v47
	v_add_f32_e32 v16, v16, v48
	v_add_f32_e32 v17, v17, v49
	v_add_f32_e32 v18, v18, v50
	v_add_f32_e32 v19, v19, v51
	v_add_f32_e32 v20, v20, v52
	v_add_f32_e32 v21, v21, v53
	v_add_f32_e32 v22, v22, v54
	v_add_f32_e32 v23, v23, v55
	v_add_f32_e32 v24, v24, v56
	v_add_f32_e32 v25, v25, v57
	v_add_f32_e32 v26, v26, v58
	v_add_f32_e32 v27, v27, v59
	v_add_f32_e32 v28, v28, v60
	v_add_f32_e32 v29, v29, v61
	v_add_f32_e32 v30, v30, v62
	v_add_f32_e32 v31, v31, v63
	v_add_f32_e32 v32, v32, v64
	v_add_f32_e32 v33, v33, v65
	v_add_f32_e32 v34, v34, v66
	v_add_f32_e32 v35, v35, v67
	v_add_f32_e32 v36, v36, v68
	v_add_f32_e32 v37, v37, v69
	v_add_f32_e32 v38, v38, v70
	v_add_f32_e32 v39, v39, v71
	ds_write_b32 v5, v8 offset:0
	ds_write_b32 v5, v9 offset:132
	ds_write_b32 v5, v10 offset:264
	ds_write_b32 v5, v11 offset:396
	ds_write_b32 v5, v12 offset:1056
	ds_write_b32 v5, v13 offset:1188
	ds_write_b32 v5, v14 offset:1320
	ds_write_b32 v5, v15 offset:1452
	ds_write_b32 v5, v16 offset:2112
	ds_write_b32 v5, v17 offset:2244
	ds_write_b32 v5, v18 offset:2376
	ds_write_b32 v5, v19 offset:2508
	ds_write_b32 v5, v20 offset:3168
	ds_write_b32 v5, v21 offset:3300
	ds_write_b32 v5, v22 offset:3432
	ds_write_b32 v5, v23 offset:3564
	ds_write_b32 v5, v24 offset:4224
	ds_write_b32 v5, v25 offset:4356
	ds_write_b32 v5, v26 offset:4488
	ds_write_b32 v5, v27 offset:4620
	ds_write_b32 v5, v28 offset:5280
	ds_write_b32 v5, v29 offset:5412
	ds_write_b32 v5, v30 offset:5544
	ds_write_b32 v5, v31 offset:5676
	ds_write_b32 v5, v32 offset:6336
	ds_write_b32 v5, v33 offset:6468
	ds_write_b32 v5, v34 offset:6600
	ds_write_b32 v5, v35 offset:6732
	ds_write_b32 v5, v36 offset:7392
	ds_write_b32 v5, v37 offset:7524
	ds_write_b32 v5, v38 offset:7656
	ds_write_b32 v5, v39 offset:7788
	s_waitcnt lgkmcnt(0)
	ds_read_b32 v8, v7 offset:0
	ds_read_b32 v9, v7 offset:4
	ds_read_b32 v10, v7 offset:8
	ds_read_b32 v11, v7 offset:12
	ds_read_b32 v12, v7 offset:16
	ds_read_b32 v13, v7 offset:20
	ds_read_b32 v14, v7 offset:24
	ds_read_b32 v15, v7 offset:28
	ds_read_b32 v16, v7 offset:32
	ds_read_b32 v17, v7 offset:36
	ds_read_b32 v18, v7 offset:40
	ds_read_b32 v19, v7 offset:44
	ds_read_b32 v20, v7 offset:48
	ds_read_b32 v21, v7 offset:52
	ds_read_b32 v22, v7 offset:56
	ds_read_b32 v23, v7 offset:60
	ds_read_b32 v24, v7 offset:64
	ds_read_b32 v25, v7 offset:68
	ds_read_b32 v26, v7 offset:72
	ds_read_b32 v27, v7 offset:76
	ds_read_b32 v28, v7 offset:80
	ds_read_b32 v29, v7 offset:84
	ds_read_b32 v30, v7 offset:88
	ds_read_b32 v31, v7 offset:92
	ds_read_b32 v32, v7 offset:96
	ds_read_b32 v33, v7 offset:100
	ds_read_b32 v34, v7 offset:104
	ds_read_b32 v35, v7 offset:108
	ds_read_b32 v36, v7 offset:112
	ds_read_b32 v37, v7 offset:116
	ds_read_b32 v38, v7 offset:120
	ds_read_b32 v39, v7 offset:124
	s_waitcnt lgkmcnt(0)
	s_and_b64 exec, exec, s[6:7]
	v_cvt_pk_f16_f32 v80, v8, v9
	v_cvt_pk_f16_f32 v81, v10, v11
	v_cvt_pk_f16_f32 v82, v12, v13
	v_cvt_pk_f16_f32 v83, v14, v15
	global_store_dwordx4 v1, v[80:83], s[30:31] offset:1088
	s_nop 1
	v_cvt_pk_f16_f32 v80, v16, v17
	v_cvt_pk_f16_f32 v81, v18, v19
	v_cvt_pk_f16_f32 v82, v20, v21
	v_cvt_pk_f16_f32 v83, v22, v23
	global_store_dwordx4 v1, v[80:83], s[30:31] offset:1104
	s_nop 1
	v_cvt_pk_f16_f32 v80, v24, v25
	v_cvt_pk_f16_f32 v81, v26, v27
	v_cvt_pk_f16_f32 v82, v28, v29
	v_cvt_pk_f16_f32 v83, v30, v31
	global_store_dwordx4 v1, v[80:83], s[30:31] offset:1120
	s_nop 1
	v_cvt_pk_f16_f32 v80, v32, v33
	v_cvt_pk_f16_f32 v81, v34, v35
	v_cvt_pk_f16_f32 v82, v36, v37
	v_cvt_pk_f16_f32 v83, v38, v39
	global_store_dwordx4 v1, v[80:83], s[30:31] offset:1136

	.amdhsa_kernel _Z13stage0_kernel5TJobs6S0Args
		.amdhsa_group_segment_fixed_size 28672
		.amdhsa_private_segment_fixed_size 0
		.amdhsa_kernarg_size 568
		.amdhsa_user_sgpr_count 2
		.amdhsa_user_sgpr_dispatch_ptr 0
		.amdhsa_user_sgpr_queue_ptr 0
		.amdhsa_user_sgpr_kernarg_segment_ptr 1
		.amdhsa_user_sgpr_dispatch_id 0
		.amdhsa_user_sgpr_kernarg_preload_length 0
		.amdhsa_user_sgpr_kernarg_preload_offset 0
		.amdhsa_user_sgpr_private_segment_size 0
		.amdhsa_uses_dynamic_stack 0
		.amdhsa_enable_private_segment 0
		.amdhsa_system_sgpr_workgroup_id_x 1
		.amdhsa_system_sgpr_workgroup_id_y 0
		.amdhsa_system_sgpr_workgroup_id_z 0
		.amdhsa_system_sgpr_workgroup_info 0
		.amdhsa_system_vgpr_workitem_id 0
		.amdhsa_next_free_vgpr 96
		.amdhsa_next_free_sgpr 100
		.amdhsa_accum_offset 96
		.amdhsa_reserve_vcc 1
		.amdhsa_float_round_mode_32 0
		.amdhsa_float_round_mode_16_64 0
		.amdhsa_float_denorm_mode_32 3
		.amdhsa_float_denorm_mode_16_64 3
		.amdhsa_dx10_clamp 1
		.amdhsa_ieee_mode 1
		.amdhsa_fp16_overflow 0
		.amdhsa_tg_split 0
		.amdhsa_exception_fp_ieee_invalid_op 0
		.amdhsa_exception_fp_denorm_src 0
		.amdhsa_exception_fp_ieee_div_zero 0
		.amdhsa_exception_fp_ieee_overflow 0
		.amdhsa_exception_fp_ieee_underflow 0
		.amdhsa_exception_fp_ieee_inexact 0
		.amdhsa_exception_int_div_zero 0
	.end_amdhsa_kernel

amdhsa.kernels:
  - .agpr_count:     0
    .args:
      - .offset:         0
        .size:           288
        .value_kind:     by_value
      - .offset:         288
        .size:           280
        .value_kind:     by_value
    .group_segment_fixed_size: 28672
    .kernarg_segment_align: 8
    .kernarg_segment_size: 568
    .language:       OpenCL C
    .language_version:
      - 2
      - 0
    .max_flat_workgroup_size: 256
    .name:           _Z13stage0_kernel5TJobs6S0Args
    .private_segment_fixed_size: 0
    .sgpr_count:     106
    .sgpr_spill_count: 213
    .symbol:         _Z13stage0_kernel5TJobs6S0Args.kd
    .uniform_work_group_size: 1
    .uses_dynamic_stack: false
    .vgpr_count:     96
    .vgpr_spill_count: 0
    .wavefront_size: 64
  - .agpr_count:     0
    .args:
      - .actual_access:  read_only
        .address_space:  global
        .offset:         0
        .size:           8
        .value_kind:     global_buffer
      - .actual_access:  read_only
        .address_space:  global
        .offset:         8
        .size:           8
        .value_kind:     global_buffer
      - .actual_access:  write_only
        .address_space:  global
        .offset:         16
        .size:           8
        .value_kind:     global_buffer
      - .offset:         24
        .size:           4
        .value_kind:     by_value
      - .offset:         28
        .size:           4
        .value_kind:     by_value
    .group_segment_fixed_size: 0
    .kernarg_segment_align: 8
    .kernarg_segment_size: 32
    .language:       OpenCL C
    .language_version:
      - 2
      - 0
    .max_flat_workgroup_size: 256
    .name:           _Z11gelu_reducePKfS0_PDF16_ii
    .private_segment_fixed_size: 0
    .sgpr_count:     18
    .sgpr_spill_count: 0
    .symbol:         _Z11gelu_reducePKfS0_PDF16_ii.kd
    .uniform_work_group_size: 1
    .uses_dynamic_stack: false
    .vgpr_count:     17
    .vgpr_spill_count: 0
    .wavefront_size: 64
  - .agpr_count:     0
    .args:
      - .address_space:  global
        .offset:         0
        .size:           8
        .value_kind:     global_buffer
      - .address_space:  global
        .offset:         8
        .size:           8
        .value_kind:     global_buffer
      - .actual_access:  read_only
        .address_space:  global
        .offset:         16
        .size:           8
        .value_kind:     global_buffer
      - .actual_access:  write_only
        .address_space:  global
        .offset:         24
        .size:           8
        .value_kind:     global_buffer
    .group_segment_fixed_size: 75776
    .kernarg_segment_align: 8
    .kernarg_segment_size: 32
    .language:       OpenCL C
    .language_version:
      - 2
      - 0
    .max_flat_workgroup_size: 512
    .name:           _Z11front_statsPKDF16_S0_PKfPf
    .private_segment_fixed_size: 0
    .sgpr_count:     18
    .sgpr_spill_count: 0
    .symbol:         _Z11front_statsPKDF16_S0_PKfPf.kd
    .uniform_work_group_size: 1
    .uses_dynamic_stack: false
    .vgpr_count:     86
    .vgpr_spill_count: 0
    .wavefront_size: 64
  - .agpr_count:     0
    .args:
      - .actual_access:  read_only
        .address_space:  global
        .offset:         0
        .size:           8
        .value_kind:     global_buffer
      - .actual_access:  read_only
        .address_space:  global
        .offset:         8
        .size:           8
        .value_kind:     global_buffer
      - .actual_access:  read_only
        .address_space:  global
        .offset:         16
        .size:           8
        .value_kind:     global_buffer
      - .actual_access:  read_only
        .address_space:  global
        .offset:         24
        .size:           8
        .value_kind:     global_buffer
      - .actual_access:  read_only
        .address_space:  global
        .offset:         32
        .size:           8
        .value_kind:     global_buffer
      - .actual_access:  read_only
        .address_space:  global
        .offset:         40
        .size:           8
        .value_kind:     global_buffer
      - .actual_access:  read_only
        .address_space:  global
        .offset:         48
        .size:           8
        .value_kind:     global_buffer
      - .actual_access:  write_only
        .address_space:  global
        .offset:         56
        .size:           8
        .value_kind:     global_buffer
    .group_segment_fixed_size: 49152
    .kernarg_segment_align: 8
    .kernarg_segment_size: 64
    .language:       OpenCL C
    .language_version:
      - 2
      - 0
    .max_flat_workgroup_size: 256
    .name:           _Z12attn2_kernelPKDF16_S0_PKfS2_S2_PKiS2_PDF16_
    .private_segment_fixed_size: 0
    .sgpr_count:     82
    .sgpr_spill_count: 0
    .symbol:         _Z12attn2_kernelPKDF16_S0_PKfS2_S2_PKiS2_PDF16_.kd
    .uniform_work_group_size: 1
    .uses_dynamic_stack: false
    .vgpr_count:     166
    .vgpr_spill_count: 0
    .wavefront_size: 64
  - .agpr_count:     0
    .args:
      - .address_space:  global
        .offset:         0
        .size:           8
        .value_kind:     global_buffer
      - .offset:         8
        .size:           4
        .value_kind:     by_value
      - .offset:         12
        .size:           4
        .value_kind:     by_value
      - .address_space:  global
        .offset:         16
        .size:           8
        .value_kind:     global_buffer
      - .offset:         24
        .size:           4
        .value_kind:     by_value
      - .offset:         28
        .size:           4
        .value_kind:     by_value
      - .offset:         32
        .size:           4
        .value_kind:     by_value
      - .offset:         36
        .size:           4
        .value_kind:     by_value
      - .offset:         40
        .size:           4
        .value_kind:     by_value
      - .actual_access:  read_only
        .address_space:  global
        .offset:         48
        .size:           8
        .value_kind:     global_buffer
      - .actual_access:  write_only
        .address_space:  global
        .offset:         56
        .size:           8
        .value_kind:     global_buffer
      - .actual_access:  write_only
        .address_space:  global
        .offset:         64
        .size:           8
        .value_kind:     global_buffer
      - .offset:         72
        .size:           4
        .value_kind:     by_value
    .group_segment_fixed_size: 73728
    .kernarg_segment_align: 8
    .kernarg_segment_size: 76
    .language:       OpenCL C
    .language_version:
      - 2
      - 0
    .max_flat_workgroup_size: 512
    .name:           _Z11gemm_kernelILi2ELi4ELi2ELi2ELi3ELi0ELi4ELb0EEvPKDF16_iiS1_iiiiiPKfPfPDF16_i
    .private_segment_fixed_size: 0
    .sgpr_count:     33
    .sgpr_spill_count: 0
    .symbol:         _Z11gemm_kernelILi2ELi4ELi2ELi2ELi3ELi0ELi4ELb0EEvPKDF16_iiS1_iiiiiPKfPfPDF16_i.kd
    .uniform_work_group_size: 1
    .uses_dynamic_stack: false
    .vgpr_count:     96
    .vgpr_spill_count: 0
    .wavefront_size: 64
  - .agpr_count:     0
    .args:
      - .address_space:  global
        .offset:         0
        .size:           8
        .value_kind:     global_buffer
      - .offset:         8
        .size:           4
        .value_kind:     by_value
      - .offset:         12
        .size:           4
        .value_kind:     by_value
      - .address_space:  global
        .offset:         16
        .size:           8
        .value_kind:     global_buffer
      - .offset:         24
        .size:           4
        .value_kind:     by_value
      - .offset:         28
        .size:           4
        .value_kind:     by_value
      - .offset:         32
        .size:           4
        .value_kind:     by_value
      - .offset:         36
        .size:           4
        .value_kind:     by_value
      - .offset:         40
        .size:           4
        .value_kind:     by_value
      - .actual_access:  read_only
        .address_space:  global
        .offset:         48
        .size:           8
        .value_kind:     global_buffer
      - .actual_access:  write_only
        .address_space:  global
        .offset:         56
        .size:           8
        .value_kind:     global_buffer
      - .actual_access:  read_only
        .address_space:  global
        .offset:         64
        .size:           8
        .value_kind:     global_buffer
      - .offset:         72
        .size:           4
        .value_kind:     by_value
    .group_segment_fixed_size: 163840
    .kernarg_segment_align: 8
    .kernarg_segment_size: 76
    .language:       OpenCL C
    .language_version:
      - 2
      - 0
    .max_flat_workgroup_size: 512
    .name:           _Z11gemm_kernelILi4ELi2ELi2ELi4ELi4ELi3ELi2ELb0EEvPKDF16_iiS1_iiiiiPKfPfPDF16_i
    .private_segment_fixed_size: 0
    .sgpr_count:     35
    .sgpr_spill_count: 0
    .symbol:         _Z11gemm_kernelILi4ELi2ELi2ELi4ELi4ELi3ELi2ELb0EEvPKDF16_iiS1_iiiiiPKfPfPDF16_i.kd
    .uniform_work_group_size: 1
    .uses_dynamic_stack: false
    .vgpr_count:     200
    .vgpr_spill_count: 0
    .wavefront_size: 64
  - .agpr_count:     0
    .args:
      - .address_space:  global
        .offset:         0
        .size:           8
        .value_kind:     global_buffer
      - .offset:         8
        .size:           4
        .value_kind:     by_value
      - .offset:         12
        .size:           4
        .value_kind:     by_value
      - .address_space:  global
        .offset:         16
        .size:           8
        .value_kind:     global_buffer
      - .offset:         24
        .size:           4
        .value_kind:     by_value
      - .offset:         28
        .size:           4
        .value_kind:     by_value
      - .offset:         32
        .size:           4
        .value_kind:     by_value
      - .offset:         36
        .size:           4
        .value_kind:     by_value
      - .offset:         40
        .size:           4
        .value_kind:     by_value
      - .actual_access:  read_only
        .address_space:  global
        .offset:         48
        .size:           8
        .value_kind:     global_buffer
      - .actual_access:  write_only
        .address_space:  global
        .offset:         56
        .size:           8
        .value_kind:     global_buffer
      - .actual_access:  read_only
        .address_space:  global
        .offset:         64
        .size:           8
        .value_kind:     global_buffer
      - .offset:         72
        .size:           4
        .value_kind:     by_value
    .group_segment_fixed_size: 65536
    .kernarg_segment_align: 8
    .kernarg_segment_size: 76
    .language:       OpenCL C
    .language_version:
      - 2
      - 0
    .max_flat_workgroup_size: 512
    .name:           _Z11gemm_kernelILi2ELi4ELi2ELi1ELi4ELi2ELi2ELb0EEvPKDF16_iiS1_iiiiiPKfPfPDF16_i
    .private_segment_fixed_size: 0
    .sgpr_count:     26
    .sgpr_spill_count: 0
    .symbol:         _Z11gemm_kernelILi2ELi4ELi2ELi1ELi4ELi2ELi2ELb0EEvPKDF16_iiS1_iiiiiPKfPfPDF16_i.kd
    .uniform_work_group_size: 1
    .uses_dynamic_stack: false
    .vgpr_count:     64
    .vgpr_spill_count: 0
    .wavefront_size: 64
